# baseline (speedup 1.0000x reference)
	.amdhsa_kernel _Z11knrm_kernelPKfS0_PKiS2_S0_Pf
		.amdhsa_group_segment_fixed_size 99712
		.amdhsa_private_segment_fixed_size 0
		.amdhsa_kernarg_size 48
		.amdhsa_user_sgpr_count 2
		.amdhsa_user_sgpr_dispatch_ptr 0
		.amdhsa_user_sgpr_queue_ptr 0
		.amdhsa_user_sgpr_kernarg_segment_ptr 1
		.amdhsa_user_sgpr_dispatch_id 0
		.amdhsa_user_sgpr_kernarg_preload_length 0
		.amdhsa_user_sgpr_kernarg_preload_offset 0
		.amdhsa_user_sgpr_private_segment_size 0
		.amdhsa_uses_dynamic_stack 0
		.amdhsa_enable_private_segment 0
		.amdhsa_system_sgpr_workgroup_id_x 1
		.amdhsa_system_sgpr_workgroup_id_y 0
		.amdhsa_system_sgpr_workgroup_id_z 0
		.amdhsa_system_sgpr_workgroup_info 0
		.amdhsa_system_vgpr_workitem_id 0
		.amdhsa_next_free_vgpr 242
		.amdhsa_next_free_sgpr 40
		.amdhsa_accum_offset 244
		.amdhsa_reserve_vcc 1
		.amdhsa_float_round_mode_32 0
		.amdhsa_float_round_mode_16_64 0
		.amdhsa_float_denorm_mode_32 3
		.amdhsa_float_denorm_mode_16_64 3
		.amdhsa_dx10_clamp 1
		.amdhsa_ieee_mode 1
		.amdhsa_fp16_overflow 0
		.amdhsa_tg_split 0
		.amdhsa_exception_fp_ieee_invalid_op 0
		.amdhsa_exception_fp_denorm_src 0
		.amdhsa_exception_fp_ieee_div_zero 0
		.amdhsa_exception_fp_ieee_overflow 0
		.amdhsa_exception_fp_ieee_underflow 0
		.amdhsa_exception_fp_ieee_inexact 0
		.amdhsa_exception_int_div_zero 0
	.end_amdhsa_kernel

amdhsa.kernels:
  - .agpr_count:     0
    .args:
      - .actual_access:  read_only
        .address_space:  global
        .offset:         0
        .size:           8
        .value_kind:     global_buffer
      - .actual_access:  read_only
        .address_space:  global
        .offset:         8
        .size:           8
        .value_kind:     global_buffer
      - .actual_access:  read_only
        .address_space:  global
        .offset:         16
        .size:           8
        .value_kind:     global_buffer
      - .actual_access:  read_only
        .address_space:  global
        .offset:         24
        .size:           8
        .value_kind:     global_buffer
      - .actual_access:  read_only
        .address_space:  global
        .offset:         32
        .size:           8
        .value_kind:     global_buffer
      - .actual_access:  write_only
        .address_space:  global
        .offset:         40
        .size:           8
        .value_kind:     global_buffer
    .group_segment_fixed_size: 99712
    .kernarg_segment_align: 8
    .kernarg_segment_size: 48
    .language:       OpenCL C
    .language_version:
      - 2
      - 0
    .max_flat_workgroup_size: 512
    .name:           _Z11knrm_kernelPKfS0_PKiS2_S0_Pf
    .private_segment_fixed_size: 0
    .sgpr_count:     46
    .sgpr_spill_count: 0
    .symbol:         _Z11knrm_kernelPKfS0_PKiS2_S0_Pf.kd
    .uniform_work_group_size: 1
    .uses_dynamic_stack: false
    .vgpr_count:     242
    .vgpr_spill_count: 0
    .wavefront_size: 64
